# mixer A tile loops: LDS-DMA request block for tile c+2 moved from behind the QK MFMAs to the end of the compute block
# speedup vs baseline: 1.0122x; 1.0023x over previous
; #define LAS __attribute__((address_space(3)))
; #define BA_TR(off_) __builtin_bit_cast(s16x4, __builtin_amdgcn_ds_read_tr16_b64_v4i16((LAS v4i16_t*)(trb + (off_))))
; #define BA_TR(off_) __builtin_bit_cast(s16x4, __builtin_amdgcn_ds_read_tr16_b64_v4i16((LAS v4i16_t*)(trb + (off_))))
; __device__ __forceinline__ void band_branch_fast(f32x16& o0, f32x16& o1, f32x4& lsum, unsigned& orw, const bf16x8 (&qf)[4], ...
;     ...
;     for (int kt = kt_lo; kt < kt_hi; ++kt) {
; #pragma unroll
;         for (int ii = 0; ii < 4; ++ii) { const int r_ = vr + 8 * ii; *(LAS v4u*)(kst + r_ * 128 + ((vc ^ (r_ & 7)) * 16)) = kn[ii]; *(LAS v4u*)(vst + r_ * 128 + vc * 16) = vn[ii]; }
;         if (kt + 1 < kt_hi) BA_LOAD(kn, vn, kt + 1);
;         bf16x8 kf[4];
; #pragma unroll
;         for (int d0 = 0; d0 < 4; ++d0) kf[d0] = *(const LAS bf16x8*)(krd + (((2 * d0 + hh) ^ (pi & 7)) * 16));
;         const LAS float* tp = tab + (kb_first + 32 * kt + tboff);
;         f32x16 s;
; #pragma unroll
;         for (int r = 0; r < 16; ++r) s[r] = tp[(r & 7) + 16 * (r >> 3)];
;         s16x4 vt[8];
; #pragma unroll
;         for (int i = 0; i < 8; ++i) vt[i] = BA_TR((i >> 2) * 2048 + ((i >> 1) & 1) * 64 + (i & 1) * 512);
;         __builtin_amdgcn_sched_barrier(0);
; #pragma unroll
;         for (int d0 = 0; d0 < 4; ++d0) s = __builtin_amdgcn_mfma_f32_32x32x16_bf16(kf[d0], qf[d0], s, 0, 0, 0);
;         __builtin_amdgcn_sched_barrier(0);
;         v4u p0, p1;
;     ...
;         p0.x = BA_PKN(s[0], s[1]); p0.y = BA_PKN(s[2], s[3]); p0.z = BA_PKN(s[4], s[5]); p0.w = BA_PKN(s[6], s[7]);
;         p1.x = BA_PKN(s[8], s[9]); p1.y = BA_PKN(s[10], s[11]); p1.z = BA_PKN(s[12], s[13]); p1.w = BA_PKN(s[14], s[15]);
;     ...
;         orw |= (p0.x | p0.y | p0.z) | (p0.w | p1.x | p1.y) | (p1.z | p1.w);
;         const bf16x8 pk0 = __builtin_bit_cast(bf16x8, p0), pk1 = __builtin_bit_cast(bf16x8, p1);
;         lsum = __builtin_amdgcn_mfma_f32_16x16x32_bf16(onesA, pk0, lsum, 0, 0, 0); lsum = __builtin_amdgcn_mfma_f32_16x16x32_bf16(onesA, pk1, lsum, 0, 0, 0);
;         o0 = __builtin_amdgcn_mfma_f32_32x32x16_bf16(BA_VF(0), pk0, o0, 0, 0, 0); o1 = __builtin_amdgcn_mfma_f32_32x32x16_bf16(BA_VF(2), pk0, o1, 0, 0, 0);
;         o0 = __builtin_amdgcn_mfma_f32_32x32x16_bf16(BA_VF(4), pk1, o0, 0, 0, 0); o1 = __builtin_amdgcn_mfma_f32_32x32x16_bf16(BA_VF(6), pk1, o1, 0, 0, 0);
.LBB0_361:
	v_add3_u32 v36, v195, v200, s99
	v_add3_u32 v37, v195, v201, s99
	ds_read_b128 v[128:131], v36 offset:20480
	ds_read_b128 v[132:135], v37 offset:20480
	v_add3_u32 v36, v195, v202, s99
	v_add3_u32 v37, v195, v203, s99
	ds_read_b128 v[164:167], v36 offset:20480
	ds_read_b128 v[168:171], v37 offset:20480
	ds_read2_b32 v[36:37], v69 offset1:1
	ds_read2_b32 v[38:39], v69 offset0:2 offset1:3
	ds_read2_b32 v[40:41], v69 offset0:4 offset1:5
	ds_read2_b32 v[42:43], v69 offset0:6 offset1:7
	ds_read2_b32 v[44:45], v69 offset0:16 offset1:17
	ds_read2_b32 v[46:47], v69 offset0:18 offset1:19
	ds_read2_b32 v[48:49], v69 offset0:20 offset1:21
	ds_read2_b32 v[50:51], v69 offset0:22 offset1:23
	v_add3_u32 v136, v194, v193, s99
	ds_read_b64_tr_b16 v[172:173], v136 offset:16384
	ds_read_b64_tr_b16 v[174:175], v136 offset:16896
	ds_read_b64_tr_b16 v[178:179], v136 offset:16960
	ds_read_b64_tr_b16 v[176:177], v136 offset:16448
	ds_read_b64_tr_b16 v[180:181], v136 offset:18432
	ds_read_b64_tr_b16 v[182:183], v136 offset:18944
	ds_read_b64_tr_b16 v[186:187], v136 offset:19008
	ds_read_b64_tr_b16 v[184:185], v136 offset:18496
	s_waitcnt lgkmcnt(8)
	v_mfma_f32_32x32x16_bf16 v[36:51], v[128:131], v[52:55], v[36:51]
	v_mfma_f32_32x32x16_bf16 v[36:51], v[132:135], v[56:59], v[36:51]
	v_mfma_f32_32x32x16_bf16 v[36:51], v[164:167], v[60:63], v[36:51]
	v_mfma_f32_32x32x16_bf16 v[36:51], v[168:171], v[64:67], v[36:51]
	s_waitcnt lgkmcnt(0)
	s_nop 11
	v_cvt_pknorm_u16_f32 v36, v36, v37
	v_cvt_pknorm_u16_f32 v37, v38, v39
	v_cvt_pknorm_u16_f32 v38, v40, v41
	v_cvt_pknorm_u16_f32 v39, v42, v43
	v_cvt_pknorm_u16_f32 v40, v44, v45
	v_cvt_pknorm_u16_f32 v41, v46, v47
	v_mfma_f32_32x32x16_bf16 v[20:35], v[172:175], v[36:39], v[20:35]
	v_cvt_pknorm_u16_f32 v42, v48, v49
	v_cvt_pknorm_u16_f32 v43, v50, v51
	v_or3_b32 v48, v127, v43, v42
	v_add_u32_e32 v69, 0x80, v69
	s_andn2_b64 vcc, exec, s[36:37]
	v_mfma_f32_32x32x16_bf16 v[4:19], v[176:179], v[36:39], v[4:19]
	v_mfma_f32_32x32x16_bf16 v[20:35], v[180:183], v[40:43], v[20:35]
	v_mfma_f32_16x16x32_bf16 v[44:47], v[70:73], v[36:39], v[90:93]
	v_or3_b32 v39, v48, v40, v39
	v_or3_b32 v37, v39, v41, v37
	v_or3_b32 v127, v37, v36, v38
	v_mfma_f32_32x32x16_bf16 v[4:19], v[184:187], v[40:43], v[4:19]
	v_mfma_f32_16x16x32_bf16 v[90:93], v[70:73], v[40:43], v[44:47]
	s_add_i32 s46, s46, 1
	s_cmp_lt_i32 s46, s16
	s_cbranch_scc0 .Lmx1_skip
	s_add_i32 m0, s98, 0x1000
	s_nop 0
	global_load_lds_dwordx4 v[94:95], off
	s_add_i32 m0, s98, 0x0
	v_lshl_add_u64 v[94:95], v[94:95], 0, s[100:101]
	global_load_lds_dwordx4 v[96:97], off
	s_add_i32 m0, s98, 0x1400
	v_lshl_add_u64 v[96:97], v[96:97], 0, s[100:101]
	global_load_lds_dwordx4 v[98:99], off
	s_add_i32 m0, s98, 0x400
	v_lshl_add_u64 v[98:99], v[98:99], 0, s[100:101]
	global_load_lds_dwordx4 v[100:101], off
	s_add_i32 m0, s98, 0x1800
	v_lshl_add_u64 v[100:101], v[100:101], 0, s[100:101]
	global_load_lds_dwordx4 v[102:103], off
	s_add_i32 m0, s98, 0x800
	v_lshl_add_u64 v[102:103], v[102:103], 0, s[100:101]
	global_load_lds_dwordx4 v[104:105], off
	s_add_i32 m0, s98, 0x1c00
	v_lshl_add_u64 v[104:105], v[104:105], 0, s[100:101]
	global_load_lds_dwordx4 v[106:107], off
	s_add_i32 m0, s98, 0xc00
	v_lshl_add_u64 v[106:107], v[106:107], 0, s[100:101]
	global_load_lds_dwordx4 v[108:109], off
	v_lshl_add_u64 v[108:109], v[108:109], 0, s[100:101]
.Lmx1_skip:
	s_add_i32 s46, s46, -1
	s_xor_b32 s98, s98, 0x2000
	s_xor_b32 s99, s99, 0x2000
	s_cbranch_vccz .LBB0_365

; #define LAS __attribute__((address_space(3)))
; #define BA_TR(off_) __builtin_bit_cast(s16x4, __builtin_amdgcn_ds_read_tr16_b64_v4i16((LAS v4i16_t*)(trb + (off_))))
; #define BA_TR(off_) __builtin_bit_cast(s16x4, __builtin_amdgcn_ds_read_tr16_b64_v4i16((LAS v4i16_t*)(trb + (off_))))
; __device__ __forceinline__ void band_branch_fast(f32x16& o0, f32x16& o1, f32x4& lsum, unsigned& orw, const bf16x8 (&qf)[4], ...
;     ...
;     for (int kt = kt_lo; kt < kt_hi; ++kt) {
; #pragma unroll
;         for (int ii = 0; ii < 4; ++ii) { const int r_ = vr + 8 * ii; *(LAS v4u*)(kst + r_ * 128 + ((vc ^ (r_ & 7)) * 16)) = kn[ii]; *(LAS v4u*)(vst + r_ * 128 + vc * 16) = vn[ii]; }
;         if (kt + 1 < kt_hi) BA_LOAD(kn, vn, kt + 1);
;         bf16x8 kf[4];
; #pragma unroll
;         for (int d0 = 0; d0 < 4; ++d0) kf[d0] = *(const LAS bf16x8*)(krd + (((2 * d0 + hh) ^ (pi & 7)) * 16));
;         const LAS float* tp = tab + (kb_first + 32 * kt + tboff);
;         f32x16 s;
; #pragma unroll
;         for (int r = 0; r < 16; ++r) s[r] = tp[(r & 7) + 16 * (r >> 3)];
;         s16x4 vt[8];
; #pragma unroll
;         for (int i = 0; i < 8; ++i) vt[i] = BA_TR((i >> 2) * 2048 + ((i >> 1) & 1) * 64 + (i & 1) * 512);
;         __builtin_amdgcn_sched_barrier(0);
; #pragma unroll
;         for (int d0 = 0; d0 < 4; ++d0) s = __builtin_amdgcn_mfma_f32_32x32x16_bf16(kf[d0], qf[d0], s, 0, 0, 0);
;         __builtin_amdgcn_sched_barrier(0);
;         v4u p0, p1;
;     ...
;         p0.x = BA_PKN(s[0], s[1]); p0.y = BA_PKN(s[2], s[3]); p0.z = BA_PKN(s[4], s[5]); p0.w = BA_PKN(s[6], s[7]);
;         p1.x = BA_PKN(s[8], s[9]); p1.y = BA_PKN(s[10], s[11]); p1.z = BA_PKN(s[12], s[13]); p1.w = BA_PKN(s[14], s[15]);
;     ...
;         orw |= (p0.x | p0.y | p0.z) | (p0.w | p1.x | p1.y) | (p1.z | p1.w);
;         const bf16x8 pk0 = __builtin_bit_cast(bf16x8, p0), pk1 = __builtin_bit_cast(bf16x8, p1);
;         lsum = __builtin_amdgcn_mfma_f32_16x16x32_bf16(onesA, pk0, lsum, 0, 0, 0); lsum = __builtin_amdgcn_mfma_f32_16x16x32_bf16(onesA, pk1, lsum, 0, 0, 0);
;         o0 = __builtin_amdgcn_mfma_f32_32x32x16_bf16(BA_VF(0), pk0, o0, 0, 0, 0); o1 = __builtin_amdgcn_mfma_f32_32x32x16_bf16(BA_VF(2), pk0, o1, 0, 0, 0);
;         o0 = __builtin_amdgcn_mfma_f32_32x32x16_bf16(BA_VF(4), pk1, o0, 0, 0, 0); o1 = __builtin_amdgcn_mfma_f32_32x32x16_bf16(BA_VF(6), pk1, o1, 0, 0, 0);
.LBB0_392:
	v_add3_u32 v5, v195, v200, s99
	v_add3_u32 v38, v195, v201, s99
	ds_read_b128 v[130:133], v5 offset:20480
	ds_read_b128 v[186:189], v38 offset:20480
	v_add3_u32 v5, v195, v202, s99
	v_add3_u32 v38, v195, v203, s99
	ds_read_b128 v[226:229], v5 offset:20480
	ds_read_b128 v[230:233], v38 offset:20480
	ds_read2_b32 v[38:39], v2 offset1:1
	ds_read2_b32 v[40:41], v2 offset0:2 offset1:3
	ds_read2_b32 v[42:43], v2 offset0:4 offset1:5
	ds_read2_b32 v[44:45], v2 offset0:6 offset1:7
	ds_read2_b32 v[46:47], v2 offset0:16 offset1:17
	ds_read2_b32 v[48:49], v2 offset0:18 offset1:19
	ds_read2_b32 v[50:51], v2 offset0:20 offset1:21
	ds_read2_b32 v[52:53], v2 offset0:22 offset1:23
	v_add3_u32 v5, v194, v193, s99
	ds_read_b64_tr_b16 v[234:235], v5 offset:16384
	ds_read_b64_tr_b16 v[236:237], v5 offset:16896
	ds_read_b64_tr_b16 v[240:241], v5 offset:16960
	ds_read_b64_tr_b16 v[238:239], v5 offset:16448
	ds_read_b64_tr_b16 v[242:243], v5 offset:18432
	ds_read_b64_tr_b16 v[244:245], v5 offset:18944
	ds_read_b64_tr_b16 v[248:249], v5 offset:19008
	ds_read_b64_tr_b16 v[246:247], v5 offset:18496
	s_waitcnt lgkmcnt(8)
	v_mfma_f32_32x32x16_bf16 v[38:53], v[130:133], v[74:77], v[38:53]
	v_mfma_f32_32x32x16_bf16 v[38:53], v[186:189], v[78:81], v[38:53]
	v_mfma_f32_32x32x16_bf16 v[38:53], v[226:229], v[82:85], v[38:53]
	v_mfma_f32_32x32x16_bf16 v[38:53], v[230:233], v[86:89], v[38:53]
	s_waitcnt lgkmcnt(0)
	s_nop 11
	v_cvt_pknorm_u16_f32 v38, v38, v39
	v_cvt_pknorm_u16_f32 v39, v40, v41
	v_cvt_pknorm_u16_f32 v40, v42, v43
	v_cvt_pknorm_u16_f32 v41, v44, v45
	v_cvt_pknorm_u16_f32 v42, v46, v47
	v_cvt_pknorm_u16_f32 v43, v48, v49
	v_mfma_f32_32x32x16_bf16 v[22:37], v[234:237], v[38:41], v[22:37]
	v_cvt_pknorm_u16_f32 v44, v50, v51
	v_cvt_pknorm_u16_f32 v45, v52, v53
	v_or3_b32 v5, v136, v45, v44
	v_or3_b32 v5, v5, v42, v41
	v_or3_b32 v5, v5, v43, v39
	v_or3_b32 v136, v5, v38, v40
	v_add_u32_e32 v2, 0x80, v2
	v_mfma_f32_32x32x16_bf16 v[6:21], v[238:241], v[38:41], v[6:21]
	s_andn2_b64 vcc, exec, s[10:11]
	v_mfma_f32_32x32x16_bf16 v[22:37], v[242:245], v[42:45], v[22:37]
	v_mfma_f32_16x16x32_bf16 v[46:49], v[70:73], v[38:41], v[54:57]
	v_mfma_f32_32x32x16_bf16 v[6:21], v[246:249], v[42:45], v[6:21]
	v_mfma_f32_16x16x32_bf16 v[54:57], v[70:73], v[42:45], v[46:49]
	s_cmp_ge_u32 s0, s35
	s_cbranch_scc1 .Lmx2_last
	s_add_i32 s0, s0, 1
	s_cmp_lt_u32 s0, s35
	s_cbranch_scc0 .Lmx2_skip
	s_add_i32 m0, s98, 0x1000
	s_nop 0
	global_load_lds_dwordx4 v[106:107], off
	s_add_i32 m0, s98, 0x0
	v_lshl_add_u64 v[106:107], v[106:107], 0, s[100:101]
	global_load_lds_dwordx4 v[108:109], off
	s_add_i32 m0, s98, 0x1400
	v_lshl_add_u64 v[108:109], v[108:109], 0, s[100:101]
	global_load_lds_dwordx4 v[110:111], off
	s_add_i32 m0, s98, 0x400
	v_lshl_add_u64 v[110:111], v[110:111], 0, s[100:101]
	global_load_lds_dwordx4 v[112:113], off
	s_add_i32 m0, s98, 0x1800
	v_lshl_add_u64 v[112:113], v[112:113], 0, s[100:101]
	global_load_lds_dwordx4 v[114:115], off
	s_add_i32 m0, s98, 0x800
	v_lshl_add_u64 v[114:115], v[114:115], 0, s[100:101]
	global_load_lds_dwordx4 v[116:117], off
	s_add_i32 m0, s98, 0x1c00
	v_lshl_add_u64 v[116:117], v[116:117], 0, s[100:101]
	global_load_lds_dwordx4 v[118:119], off
	s_add_i32 m0, s98, 0xc00
	v_lshl_add_u64 v[118:119], v[118:119], 0, s[100:101]
	global_load_lds_dwordx4 v[120:121], off
	v_lshl_add_u64 v[120:121], v[120:121], 0, s[100:101]

; #define LAS __attribute__((address_space(3)))
; #define BA_TR(off_) __builtin_bit_cast(s16x4, __builtin_amdgcn_ds_read_tr16_b64_v4i16((LAS v4i16_t*)(trb + (off_))))
; #define BA_TR(off_) __builtin_bit_cast(s16x4, __builtin_amdgcn_ds_read_tr16_b64_v4i16((LAS v4i16_t*)(trb + (off_))))
; __device__ __forceinline__ void band_branch_fast(f32x16& o0, f32x16& o1, f32x4& lsum, unsigned& orw, const bf16x8 (&qf)[4], ...
;     ...
;     for (int kt = kt_lo; kt < kt_hi; ++kt) {
; #pragma unroll
;         for (int ii = 0; ii < 4; ++ii) { const int r_ = vr + 8 * ii; *(LAS v4u*)(kst + r_ * 128 + ((vc ^ (r_ & 7)) * 16)) = kn[ii]; *(LAS v4u*)(vst + r_ * 128 + vc * 16) = vn[ii]; }
;         if (kt + 1 < kt_hi) BA_LOAD(kn, vn, kt + 1);
;         bf16x8 kf[4];
; #pragma unroll
;         for (int d0 = 0; d0 < 4; ++d0) kf[d0] = *(const LAS bf16x8*)(krd + (((2 * d0 + hh) ^ (pi & 7)) * 16));
;         const LAS float* tp = tab + (kb_first + 32 * kt + tboff);
;         f32x16 s;
; #pragma unroll
;         for (int r = 0; r < 16; ++r) s[r] = tp[(r & 7) + 16 * (r >> 3)];
;         s16x4 vt[8];
; #pragma unroll
;         for (int i = 0; i < 8; ++i) vt[i] = BA_TR((i >> 2) * 2048 + ((i >> 1) & 1) * 64 + (i & 1) * 512);
;         __builtin_amdgcn_sched_barrier(0);
; #pragma unroll
;         for (int d0 = 0; d0 < 4; ++d0) s = __builtin_amdgcn_mfma_f32_32x32x16_bf16(kf[d0], qf[d0], s, 0, 0, 0);
;         __builtin_amdgcn_sched_barrier(0);
;         v4u p0, p1;
;     ...
;         p0.x = BA_PKN(s[0], s[1]); p0.y = BA_PKN(s[2], s[3]); p0.z = BA_PKN(s[4], s[5]); p0.w = BA_PKN(s[6], s[7]);
;         p1.x = BA_PKN(s[8], s[9]); p1.y = BA_PKN(s[10], s[11]); p1.z = BA_PKN(s[12], s[13]); p1.w = BA_PKN(s[14], s[15]);
;     ...
;         orw |= (p0.x | p0.y | p0.z) | (p0.w | p1.x | p1.y) | (p1.z | p1.w);
;         const bf16x8 pk0 = __builtin_bit_cast(bf16x8, p0), pk1 = __builtin_bit_cast(bf16x8, p1);
;         lsum = __builtin_amdgcn_mfma_f32_16x16x32_bf16(onesA, pk0, lsum, 0, 0, 0); lsum = __builtin_amdgcn_mfma_f32_16x16x32_bf16(onesA, pk1, lsum, 0, 0, 0);
;         o0 = __builtin_amdgcn_mfma_f32_32x32x16_bf16(BA_VF(0), pk0, o0, 0, 0, 0); o1 = __builtin_amdgcn_mfma_f32_32x32x16_bf16(BA_VF(2), pk0, o1, 0, 0, 0);
;         o0 = __builtin_amdgcn_mfma_f32_32x32x16_bf16(BA_VF(4), pk1, o0, 0, 0, 0); o1 = __builtin_amdgcn_mfma_f32_32x32x16_bf16(BA_VF(6), pk1, o1, 0, 0, 0);
.Lmx3_p1b:
.Lmx2_join:
	s_cbranch_vccz .LBB0_396

; #define LAS __attribute__((address_space(3)))
; #define BA_TR(off_) __builtin_bit_cast(s16x4, __builtin_amdgcn_ds_read_tr16_b64_v4i16((LAS v4i16_t*)(trb + (off_))))
; #define BA_TR(off_) __builtin_bit_cast(s16x4, __builtin_amdgcn_ds_read_tr16_b64_v4i16((LAS v4i16_t*)(trb + (off_))))
; __device__ __forceinline__ void band_branch_fast(f32x16& o0, f32x16& o1, f32x4& lsum, unsigned& orw, const bf16x8 (&qf)[4], ...
;     ...
;     for (int kt = kt_lo; kt < kt_hi; ++kt) {
; #pragma unroll
;         for (int ii = 0; ii < 4; ++ii) { const int r_ = vr + 8 * ii; *(LAS v4u*)(kst + r_ * 128 + ((vc ^ (r_ & 7)) * 16)) = kn[ii]; *(LAS v4u*)(vst + r_ * 128 + vc * 16) = vn[ii]; }
;         if (kt + 1 < kt_hi) BA_LOAD(kn, vn, kt + 1);
;         bf16x8 kf[4];
; #pragma unroll
;         for (int d0 = 0; d0 < 4; ++d0) kf[d0] = *(const LAS bf16x8*)(krd + (((2 * d0 + hh) ^ (pi & 7)) * 16));
;         const LAS float* tp = tab + (kb_first + 32 * kt + tboff);
;         f32x16 s;
; #pragma unroll
;         for (int r = 0; r < 16; ++r) s[r] = tp[(r & 7) + 16 * (r >> 3)];
;         s16x4 vt[8];
; #pragma unroll
;         for (int i = 0; i < 8; ++i) vt[i] = BA_TR((i >> 2) * 2048 + ((i >> 1) & 1) * 64 + (i & 1) * 512);
;         __builtin_amdgcn_sched_barrier(0);
; #pragma unroll
;         for (int d0 = 0; d0 < 4; ++d0) s = __builtin_amdgcn_mfma_f32_32x32x16_bf16(kf[d0], qf[d0], s, 0, 0, 0);
;         __builtin_amdgcn_sched_barrier(0);
;         v4u p0, p1;
;     ...
;         p0.x = BA_PKN(s[0], s[1]); p0.y = BA_PKN(s[2], s[3]); p0.z = BA_PKN(s[4], s[5]); p0.w = BA_PKN(s[6], s[7]);
;         p1.x = BA_PKN(s[8], s[9]); p1.y = BA_PKN(s[10], s[11]); p1.z = BA_PKN(s[12], s[13]); p1.w = BA_PKN(s[14], s[15]);
;     ...
;         orw |= (p0.x | p0.y | p0.z) | (p0.w | p1.x | p1.y) | (p1.z | p1.w);
;         const bf16x8 pk0 = __builtin_bit_cast(bf16x8, p0), pk1 = __builtin_bit_cast(bf16x8, p1);
;         lsum = __builtin_amdgcn_mfma_f32_16x16x32_bf16(onesA, pk0, lsum, 0, 0, 0); lsum = __builtin_amdgcn_mfma_f32_16x16x32_bf16(onesA, pk1, lsum, 0, 0, 0);
;         o0 = __builtin_amdgcn_mfma_f32_32x32x16_bf16(BA_VF(0), pk0, o0, 0, 0, 0); o1 = __builtin_amdgcn_mfma_f32_32x32x16_bf16(BA_VF(2), pk0, o1, 0, 0, 0);
;         o0 = __builtin_amdgcn_mfma_f32_32x32x16_bf16(BA_VF(4), pk1, o0, 0, 0, 0); o1 = __builtin_amdgcn_mfma_f32_32x32x16_bf16(BA_VF(6), pk1, o1, 0, 0, 0);
.LBB0_397:
	v_add3_u32 v38, v195, v200, s99
	v_add3_u32 v39, v195, v201, s99
	ds_read_b128 v[186:189], v38 offset:20480
	ds_read_b128 v[226:229], v39 offset:20480
	v_add3_u32 v38, v195, v202, s99
	v_add3_u32 v39, v195, v203, s99
	ds_read_b128 v[230:233], v38 offset:20480
	ds_read_b128 v[234:237], v39 offset:20480
	ds_read2_b32 v[38:39], v2 offset1:1
	ds_read2_b32 v[40:41], v2 offset0:2 offset1:3
	ds_read2_b32 v[42:43], v2 offset0:4 offset1:5
	ds_read2_b32 v[44:45], v2 offset0:6 offset1:7
	ds_read2_b32 v[46:47], v2 offset0:16 offset1:17
	ds_read2_b32 v[48:49], v2 offset0:18 offset1:19
	ds_read2_b32 v[50:51], v2 offset0:20 offset1:21
	ds_read2_b32 v[52:53], v2 offset0:22 offset1:23
	v_add3_u32 v137, v194, v193, s99
	ds_read_b64_tr_b16 v[238:239], v137 offset:16384
	ds_read_b64_tr_b16 v[240:241], v137 offset:16896
	ds_read_b64_tr_b16 v[244:245], v137 offset:16960
	ds_read_b64_tr_b16 v[242:243], v137 offset:16448
	ds_read_b64_tr_b16 v[246:247], v137 offset:18432
	ds_read_b64_tr_b16 v[248:249], v137 offset:18944
	ds_read_b64_tr_b16 v[252:253], v137 offset:19008
	ds_read_b64_tr_b16 v[250:251], v137 offset:18496
	s_waitcnt lgkmcnt(8)
	v_mfma_f32_32x32x16_bf16 v[38:53], v[186:189], v[74:77], v[38:53]
	v_mfma_f32_32x32x16_bf16 v[38:53], v[226:229], v[78:81], v[38:53]
	v_mfma_f32_32x32x16_bf16 v[38:53], v[230:233], v[82:85], v[38:53]
	v_mfma_f32_32x32x16_bf16 v[38:53], v[234:237], v[86:89], v[38:53]
	s_waitcnt lgkmcnt(0)
	s_nop 11
	v_cvt_pknorm_u16_f32 v38, v38, v39
	v_cvt_pknorm_u16_f32 v39, v40, v41
	v_cvt_pknorm_u16_f32 v40, v42, v43
	v_cvt_pknorm_u16_f32 v41, v44, v45
	v_cvt_pknorm_u16_f32 v42, v46, v47
	v_cvt_pknorm_u16_f32 v43, v48, v49
	v_mfma_f32_32x32x16_bf16 v[22:37], v[238:241], v[38:41], v[22:37]
	v_cvt_pknorm_u16_f32 v44, v50, v51
	v_cvt_pknorm_u16_f32 v45, v52, v53
	v_or3_b32 v50, v136, v45, v44
	v_add_u32_e32 v2, 0x80, v2
	v_mfma_f32_32x32x16_bf16 v[6:21], v[242:245], v[38:41], v[6:21]
	s_andn2_b64 vcc, exec, s[10:11]
	v_mfma_f32_16x16x32_bf16 v[46:49], v[70:73], v[38:41], v[54:57]
	v_or3_b32 v41, v50, v42, v41
	v_or3_b32 v39, v41, v43, v39
	v_or3_b32 v136, v39, v38, v40
	v_mfma_f32_32x32x16_bf16 v[22:37], v[246:249], v[42:45], v[22:37]
	v_mfma_f32_32x32x16_bf16 v[6:21], v[250:253], v[42:45], v[6:21]
	v_mfma_f32_16x16x32_bf16 v[54:57], v[70:73], v[42:45], v[46:49]
	s_add_i32 s0, s0, 1
	s_cmp_lt_u32 s0, s37
	s_cbranch_scc0 .Lmx3_skip
	s_add_i32 m0, s98, 0x1000
	s_nop 0
	global_load_lds_dwordx4 v[106:107], off
	s_add_i32 m0, s98, 0x0
	v_lshl_add_u64 v[106:107], v[106:107], 0, s[20:21]
	global_load_lds_dwordx4 v[108:109], off
	s_add_i32 m0, s98, 0x1400
	v_lshl_add_u64 v[108:109], v[108:109], 0, s[20:21]
	global_load_lds_dwordx4 v[110:111], off
	s_add_i32 m0, s98, 0x400
	v_lshl_add_u64 v[110:111], v[110:111], 0, s[20:21]
	global_load_lds_dwordx4 v[112:113], off
	s_add_i32 m0, s98, 0x1800
	v_lshl_add_u64 v[112:113], v[112:113], 0, s[20:21]
	global_load_lds_dwordx4 v[114:115], off
	s_add_i32 m0, s98, 0x800
	v_lshl_add_u64 v[114:115], v[114:115], 0, s[20:21]
	global_load_lds_dwordx4 v[116:117], off
	s_add_i32 m0, s98, 0x1c00
	v_lshl_add_u64 v[116:117], v[116:117], 0, s[20:21]
	global_load_lds_dwordx4 v[118:119], off
	s_add_i32 m0, s98, 0xc00
	v_lshl_add_u64 v[118:119], v[118:119], 0, s[20:21]
	global_load_lds_dwordx4 v[120:121], off
	v_lshl_add_u64 v[120:121], v[120:121], 0, s[20:21]
.Lmx3_skip:
	s_add_i32 s0, s0, -1
	s_xor_b32 s98, s98, 0x2000
	s_xor_b32 s99, s99, 0x2000
	s_cbranch_vccz .LBB0_400
